# split-phase grid barrier 4 for workgroups 0-63: arrive, run the remaining P GEMM units (independent of phase 3), wait only before the pooling GEMM; on top of the split barrier 1
# baseline (speedup 1.0000x reference)
; __global__ void __launch_bounds__(NTHREADS, 2) fwd(Params p) {
;     ...
;     xcd_barrier(bar, wave);
;     if (PROBE == 3) { phase3(p, lds, wave); xcd_barrier(bar, wave); }
;     {
;         pg8::Gemm g{(const bf16_t*)p.hb, (const bf16_t*)p.wt_in, ND / 2, ND / 2, ND / 2}; WinRestOrder S{bid, (size_t)256 * ND, (size_t)256 * ND};
;         EpiP E{p.P}; pg8::gemm_phase<EpiP, WinRestOrder, true>(lds, g, S, E, wave); }
.Lmy_gb4_wait:
	v_readlane_b32 s2, v254, 3
	s_cmp_lt_u32 s2, 64
	s_cbranch_scc1 .Lmy_gb4_out
	v_mov_b32_e32 v0, 0
	s_mov_b32 s2, 0

; __device__ __forceinline__ unsigned xb_ld(unsigned* p)              { return __hip_atomic_load(p, __ATOMIC_RELAXED, __HIP_MEMORY_SCOPE_AGENT); }
; __device__ __forceinline__ unsigned xb_add(unsigned* p, unsigned v) { return __hip_atomic_fetch_add(p, v, __ATOMIC_RELAXED, __HIP_MEMORY_SCOPE_AGENT); }
; #define XB_SPIN(cond, bar) do { unsigned _sp = 0; while (cond) { __builtin_amdgcn_s_sleep(1); \
;     if ((++_sp & 255u) == 0u) { if (xb_ld(&(bar)[XB_TMO])) break; if (_sp > XB_SPIN_CAP) { atomicAdd(&(bar)[XB_TMO], 1u); break; } } } } while (0)
; __device__ __forceinline__ void xcd_barrier(const XcdBarrier& b, const int wave) {
;     ...
;             else XB_SPIN(xb_ld(&bar[XB_TOPGEN]) == tg, bar);
;             __builtin_amdgcn_fence(__ATOMIC_ACQUIRE, "agent");
;             xb_add(&bar[XB_XGEN(b.x)], 1u);
;             asm volatile("s_waitcnt vmcnt(0)" ::: "memory");
;         } else {
;             XB_SPIN(xb_ld(&bar[XB_XGEN(b.x)]) == gen, bar);
;             __builtin_amdgcn_fence(__ATOMIC_ACQUIRE, "agent");
;             asm volatile("s_waitcnt vmcnt(0)" ::: "memory");
; __global__ void __launch_bounds__(NTHREADS, 2) fwd(Params p) {
;     ...
;     __syncthreads();
;     {
;         pg8::Gemm g{p.dp, p.wt_pool, NC, 256, 256}; PoolOrder S{1 << 20, bid >= 64 ? bid - 64 : 192 + bid};
.LBB0_429:
	v_readlane_b32 s98, v255, 29
	s_cmp_lg_u32 s98, 0
	s_cbranch_scc1 .Lmy_b4w_done
	s_mov_b64 s[98:99], exec
	s_mov_b64 exec, 1
	v_readlane_b32 s100, v254, 36
	v_readlane_b32 s101, v254, 37
	v_mov_b32_e32 v0, 0
	s_mov_b32 s10, 0
	s_nop 2
.Lmy_b4w_poll:
	global_load_dwordx4 v[2:5], v0, s[100:101] sc1
	global_load_dwordx4 v[6:9], v0, s[100:101] offset:16 sc1
	s_waitcnt vmcnt(0)
	v_min_u32_e32 v2, v2, v3
	v_min_u32_e32 v4, v4, v5
	v_min_u32_e32 v6, v6, v7
	v_min_u32_e32 v8, v8, v9
	v_min_u32_e32 v2, v2, v4
	v_min_u32_e32 v6, v6, v8
	v_min_u32_e32 v1, v2, v6
	v_cmp_gt_u32_e32 vcc, 4, v1
	s_cbranch_vccz .Lmy_b4w_ok
	s_sleep 1
	s_add_u32 s10, s10, 1
	s_cmp_lt_u32 s10, 0x40000
	s_cbranch_scc1 .Lmy_b4w_poll
.Lmy_b4w_ok:
	buffer_inv sc1
	s_waitcnt vmcnt(0)
	s_mov_b64 exec, s[98:99]
